# plus: P3 latent-chunk XBC tile request loads non-temporal
# speedup vs baseline: 1.0197x; 1.0039x over previous
; __global__ void __launch_bounds__(NWAVES * 64, 2) mk_fwd(Args args) {
;     ...
;         if (item < NCHUNK * 8 && (item >> 3) < 128) P3_REQUEST(item);
.LBB0_554:
	s_lshr_b32 s7, s65, 7
	v_mov_b32_e32 v189, 0
	s_andn2_b64 vcc, exec, s[2:3]
	v_mov_b32_e32 v190, 0
	v_mov_b32_e32 v191, 0
	s_cbranch_vccnz .LBB0_556
	v_mov_b32_e32 v1, v0
	s_and_b32 s11, s10, 1
	s_lshl_b32 s8, s8, 7
	s_bfe_u32 s9, s10, 0x20001
	v_ashrrev_i32_e32 v2, 4, v1
	s_lshl_b32 s2, s11, 2
	v_add_u32_e32 v4, s8, v2
	s_movk_i32 s13, 0x1800
	v_mov_b64_e32 v[2:3], s[4:5]
	v_add_u32_e32 v11, 0x200, v1
	s_add_i32 s12, s2, s7
	v_mad_i64_i32 v[4:5], s[2:3], v4, s13, v[2:3]
	s_lshl_b32 s16, s9, 8
	s_mov_b32 s17, 0
	v_lshlrev_b32_e32 v10, 4, v1
	v_ashrrev_i32_e32 v8, 4, v11
	v_lshl_add_u64 v[4:5], v[4:5], 0, s[16:17]
	v_and_b32_e32 v6, 0xf0, v10
	v_mov_b32_e32 v7, 0
	v_add_u32_e32 v8, s8, v8
	v_lshl_add_u64 v[4:5], v[4:5], 0, v[6:7]
	s_mov_b32 s14, 0x12801000
	v_mad_i64_i32 v[8:9], s[2:3], v8, s13, v[2:3]
	v_add_co_u32_e32 v4, vcc, s14, v4
	v_lshl_add_u64 v[8:9], v[8:9], 0, s[16:17]
	s_nop 0
	v_addc_co_u32_e32 v5, vcc, 0, v5, vcc
	v_lshl_add_u64 v[8:9], v[8:9], 0, v[6:7]
	v_add_co_u32_e32 v8, vcc, s14, v8
	s_nop 1
	v_addc_co_u32_e32 v9, vcc, 0, v9, vcc
	global_load_dwordx4 v[130:133], v[4:5], off nt
	global_load_dwordx4 v[134:137], v[8:9], off nt
	v_add_u32_e32 v8, 0x400, v1
	v_ashrrev_i32_e32 v4, 4, v8
	v_add_u32_e32 v4, s8, v4
	v_add_u32_e32 v9, 0x600, v1
	v_mad_i64_i32 v[4:5], s[2:3], v4, s13, v[2:3]
	v_ashrrev_i32_e32 v12, 4, v9
	v_lshl_add_u64 v[4:5], v[4:5], 0, s[16:17]
	v_add_u32_e32 v12, s8, v12
	v_lshl_add_u64 v[4:5], v[4:5], 0, v[6:7]
	v_mad_i64_i32 v[2:3], s[2:3], v12, s13, v[2:3]
	v_add_co_u32_e32 v4, vcc, s14, v4
	v_lshl_add_u64 v[2:3], v[2:3], 0, s[16:17]
	s_nop 0
	v_addc_co_u32_e32 v5, vcc, 0, v5, vcc
	v_lshl_add_u64 v[2:3], v[2:3], 0, v[6:7]
	v_add_co_u32_e32 v2, vcc, s14, v2
	s_lshl_b32 s14, s9, 3
	s_lshl_b32 s2, s9, 10
	s_add_u32 s2, s4, s2
	s_addc_u32 s3, s5, 0
	s_lshl_b32 s9, s11, 9
	s_add_u32 s2, s2, s9
	v_addc_co_u32_e32 v3, vcc, 0, v3, vcc
	s_addc_u32 s3, s3, 0
	v_and_b32_e32 v6, 0x1f0, v10
	global_load_dwordx4 v[138:141], v[4:5], off nt
	global_load_dwordx4 v[142:145], v[2:3], off nt
	v_lshl_add_u64 v[2:3], s[2:3], 0, v[6:7]
	s_mov_b64 s[2:3], 0x12800000
	v_ashrrev_i32_e32 v4, 5, v1
	v_ashrrev_i32_e32 v6, 5, v11
	v_lshl_add_u64 v[2:3], v[2:3], 0, s[2:3]
	v_add_u32_e32 v4, s8, v4
	v_add_u32_e32 v6, s8, v6
	v_mad_i64_i32 v[4:5], s[2:3], v4, s13, v[2:3]
	v_mad_i64_i32 v[6:7], s[2:3], v6, s13, v[2:3]
	global_load_dwordx4 v[146:149], v[4:5], off nt
	global_load_dwordx4 v[150:153], v[6:7], off nt
	v_ashrrev_i32_e32 v4, 5, v8
	v_ashrrev_i32_e32 v6, 5, v9
	v_add_u32_e32 v4, s8, v4
	v_add_u32_e32 v6, s8, v6
	v_mad_i64_i32 v[4:5], s[2:3], v4, s13, v[2:3]
	v_mad_i64_i32 v[6:7], s[2:3], v6, s13, v[2:3]
	global_load_dwordx4 v[154:157], v[4:5], off nt
	global_load_dwordx4 v[158:161], v[6:7], off nt
	v_add_u32_e32 v4, 0x800, v1
	v_add_u32_e32 v6, 0xa00, v1
	v_ashrrev_i32_e32 v4, 5, v4
	v_ashrrev_i32_e32 v6, 5, v6
	v_add_u32_e32 v4, s8, v4
	v_add_u32_e32 v6, s8, v6
	v_mad_i64_i32 v[4:5], s[2:3], v4, s13, v[2:3]
	v_mad_i64_i32 v[6:7], s[2:3], v6, s13, v[2:3]
	global_load_dwordx4 v[162:165], v[4:5], off nt
	global_load_dwordx4 v[166:169], v[6:7], off nt
	v_add_u32_e32 v4, 0xc00, v1
	v_add_u32_e32 v6, 0xe00, v1
	v_ashrrev_i32_e32 v4, 5, v4
	v_ashrrev_i32_e32 v6, 5, v6
	v_add_u32_e32 v4, s8, v4
	v_add_u32_e32 v6, s8, v6
	v_lshlrev_b32_e32 v1, 1, v1
	v_mad_i64_i32 v[4:5], s[2:3], v4, s13, v[2:3]
	v_mad_i64_i32 v[2:3], s[2:3], v6, s13, v[2:3]
	v_and_b32_e32 v1, 0x7e, v1
	global_load_dwordx4 v[170:173], v[4:5], off nt
	global_load_dwordx4 v[174:177], v[2:3], off nt
	v_or_b32_e32 v2, s8, v1
	s_add_i32 s12, s12, s14
	v_ashrrev_i32_e32 v3, 31, v2
	s_add_u32 s2, s4, 0xb00000
	v_lshlrev_b64 v[4:5], 8, v[2:3]
	v_or_b32_e32 v2, 1, v2
	s_addc_u32 s3, s5, 0
	v_ashrrev_i32_e32 v3, 31, v2
	v_lshl_add_u64 v[4:5], s[2:3], 0, v[4:5]
	s_lshl_b32 s8, s6, 7
	s_mov_b32 s9, s17
	v_lshlrev_b64 v[2:3], 8, v[2:3]
	v_lshl_add_u64 v[4:5], v[4:5], 0, s[8:9]
	s_lshl_b32 s12, s12, 2
	s_mov_b32 s13, s17
	v_lshl_add_u64 v[2:3], s[2:3], 0, v[2:3]
	v_lshl_add_u64 v[4:5], v[4:5], 0, s[12:13]
	v_lshl_add_u64 v[2:3], v[2:3], 0, s[8:9]
	v_lshl_add_u64 v[2:3], v[2:3], 0, s[12:13]
	global_load_dword v190, v[4:5], off
	global_load_dword v191, v[2:3], off
	s_lshl_b32 s16, s6, 5

; __global__ void __launch_bounds__(NWAVES * 64, 2) mk_fwd(Args args) {
;     ...
;             __syncthreads();
;             if (nitem < NCHUNK * 8 && (nitem >> 3) < 128) P3_REQUEST(nitem);
.LBB0_568:
	s_or_b64 exec, exec, s[2:3]
	s_cmpk_gt_i32 s52, 0x43f
	s_cselect_b64 s[2:3], -1, 0
	s_and_b64 vcc, exec, s[2:3]
	s_waitcnt lgkmcnt(0)
	s_barrier
	s_cbranch_vccnz .LBB0_571
	s_ashr_i32 s10, s52, 3
	s_cmpk_gt_i32 s10, 0x7f
	s_cbranch_scc1 .LBB0_571
	v_mov_b32_e32 v10, v0
	s_and_b32 s13, s52, 1
	s_lshl_b32 s15, s10, 7
	s_bfe_u32 s12, s52, 0x20001
	v_ashrrev_i32_e32 v2, 4, v10
	s_lshl_b32 s11, s13, 2
	v_add_u32_e32 v4, s15, v2
	v_mov_b64_e32 v[2:3], s[4:5]
	v_add_u32_e32 v12, 0x200, v10
	s_add_i32 s14, s11, s7
	v_mad_i64_i32 v[4:5], s[10:11], v4, s40, v[2:3]
	s_lshl_b32 s18, s12, 8
	v_lshlrev_b32_e32 v11, 4, v10
	v_ashrrev_i32_e32 v8, 4, v12
	v_lshl_add_u64 v[4:5], v[4:5], 0, s[18:19]
	v_and_b32_e32 v6, 0xf0, v11
	v_mov_b32_e32 v7, v189
	v_add_u32_e32 v8, s15, v8
	v_lshl_add_u64 v[4:5], v[4:5], 0, v[6:7]
	v_mad_i64_i32 v[8:9], s[10:11], v8, s40, v[2:3]
	v_add_co_u32_e32 v4, vcc, s50, v4
	v_lshl_add_u64 v[8:9], v[8:9], 0, s[18:19]
	s_nop 0
	v_addc_co_u32_e32 v5, vcc, 0, v5, vcc
	v_lshl_add_u64 v[8:9], v[8:9], 0, v[6:7]
	v_add_co_u32_e32 v8, vcc, s50, v8
	s_nop 1
	v_addc_co_u32_e32 v9, vcc, 0, v9, vcc
	global_load_dwordx4 v[130:133], v[4:5], off nt
	global_load_dwordx4 v[134:137], v[8:9], off nt
	v_add_u32_e32 v8, 0x400, v10
	v_ashrrev_i32_e32 v4, 4, v8
	v_add_u32_e32 v4, s15, v4
	v_add_u32_e32 v9, 0x600, v10
	v_mad_i64_i32 v[4:5], s[10:11], v4, s40, v[2:3]
	v_ashrrev_i32_e32 v13, 4, v9
	v_lshl_add_u64 v[4:5], v[4:5], 0, s[18:19]
	v_add_u32_e32 v13, s15, v13
	v_lshl_add_u64 v[4:5], v[4:5], 0, v[6:7]
	v_mad_i64_i32 v[2:3], s[10:11], v13, s40, v[2:3]
	v_add_co_u32_e32 v4, vcc, s50, v4
	v_lshl_add_u64 v[2:3], v[2:3], 0, s[18:19]
	s_lshl_b32 s18, s12, 3
	s_lshl_b32 s10, s12, 10
	v_addc_co_u32_e32 v5, vcc, 0, v5, vcc
	v_lshl_add_u64 v[2:3], v[2:3], 0, v[6:7]
	s_add_u32 s10, s35, s10
	v_add_co_u32_e32 v2, vcc, s50, v2
	s_addc_u32 s11, s36, 0
	s_lshl_b32 s12, s13, 9
	v_addc_co_u32_e32 v3, vcc, 0, v3, vcc
	s_add_u32 s10, s10, s12
	global_load_dwordx4 v[138:141], v[4:5], off nt
	global_load_dwordx4 v[142:145], v[2:3], off nt
	s_addc_u32 s11, s11, 0
	v_and_b32_e32 v2, 0x1f0, v11
	v_mov_b32_e32 v3, v189
	v_ashrrev_i32_e32 v4, 5, v10
	v_ashrrev_i32_e32 v6, 5, v12
	v_lshl_add_u64 v[2:3], s[10:11], 0, v[2:3]
	v_add_u32_e32 v4, s15, v4
	v_add_u32_e32 v6, s15, v6
	v_mad_i64_i32 v[4:5], s[10:11], v4, s40, v[2:3]
	v_mad_i64_i32 v[6:7], s[10:11], v6, s40, v[2:3]
	global_load_dwordx4 v[146:149], v[4:5], off nt
	global_load_dwordx4 v[150:153], v[6:7], off nt
	v_ashrrev_i32_e32 v4, 5, v8
	v_ashrrev_i32_e32 v6, 5, v9
	v_add_u32_e32 v4, s15, v4
	v_add_u32_e32 v6, s15, v6
	v_mad_i64_i32 v[4:5], s[10:11], v4, s40, v[2:3]
	v_mad_i64_i32 v[6:7], s[10:11], v6, s40, v[2:3]
	global_load_dwordx4 v[154:157], v[4:5], off nt
	global_load_dwordx4 v[158:161], v[6:7], off nt
	v_add_u32_e32 v4, 0x800, v10
	v_add_u32_e32 v6, 0xa00, v10
	v_ashrrev_i32_e32 v4, 5, v4
	v_ashrrev_i32_e32 v6, 5, v6
	v_add_u32_e32 v4, s15, v4
	v_add_u32_e32 v6, s15, v6
	v_mad_i64_i32 v[4:5], s[10:11], v4, s40, v[2:3]
	v_mad_i64_i32 v[6:7], s[10:11], v6, s40, v[2:3]
	global_load_dwordx4 v[162:165], v[4:5], off nt
	global_load_dwordx4 v[166:169], v[6:7], off nt
	v_add_u32_e32 v4, 0xc00, v10
	v_add_u32_e32 v6, 0xe00, v10
	v_ashrrev_i32_e32 v4, 5, v4
	v_ashrrev_i32_e32 v6, 5, v6
	v_add_u32_e32 v4, s15, v4
	v_add_u32_e32 v6, s15, v6
	v_mad_i64_i32 v[4:5], s[10:11], v4, s40, v[2:3]
	v_mad_i64_i32 v[2:3], s[10:11], v6, s40, v[2:3]
	global_load_dwordx4 v[170:173], v[4:5], off nt
	global_load_dwordx4 v[174:177], v[2:3], off nt
	v_lshlrev_b32_e32 v2, 1, v10
	v_and_b32_e32 v2, 0x7e, v2
	v_or_b32_e32 v2, s15, v2
	v_ashrrev_i32_e32 v3, 31, v2
	v_lshlrev_b64 v[4:5], 8, v[2:3]
	v_or_b32_e32 v2, 1, v2
	s_add_i32 s14, s14, s18
	v_ashrrev_i32_e32 v3, 31, v2
	v_lshl_add_u64 v[4:5], s[20:21], 0, v[4:5]
	s_lshl_b32 s18, s14, 2
	v_lshlrev_b64 v[2:3], 8, v[2:3]
	v_lshl_add_u64 v[4:5], v[4:5], 0, s[18:19]
	v_lshl_add_u64 v[2:3], s[20:21], 0, v[2:3]
	v_lshl_add_u64 v[2:3], v[2:3], 0, s[18:19]
	global_load_dword v190, v[4:5], off
	global_load_dword v191, v[2:3], off
